# DeltaNet recurrence: 43 of the 48 half-wave register exchanges now by v_permlane32_swap
# baseline (speedup 1.0000x reference)
.LBB0_800:
	v_lshlrev_b32_e32 v36, 16, v158
	v_and_b32_e32 v37, 0xffff0000, v158
	v_lshlrev_b32_e32 v38, 16, v159
	v_and_b32_e32 v39, 0xffff0000, v159
	v_lshlrev_b32_e32 v40, 16, v154
	v_and_b32_e32 v41, 0xffff0000, v154
	v_lshlrev_b32_e32 v42, 16, v155
	v_and_b32_e32 v43, 0xffff0000, v155
	v_lshlrev_b32_e32 v44, 16, v152
	v_and_b32_e32 v45, 0xffff0000, v152
	v_lshlrev_b32_e32 v46, 16, v153
	v_and_b32_e32 v47, 0xffff0000, v153
	v_lshlrev_b32_e32 v48, 16, v150
	v_and_b32_e32 v49, 0xffff0000, v150
	v_lshlrev_b32_e32 v50, 16, v151
	v_and_b32_e32 v51, 0xffff0000, v151
	v_cvt_pk_bf16_f32 v116, -v20, -v21
	v_cvt_pk_bf16_f32 v117, -v22, -v23
	v_cvt_pk_bf16_f32 v118, -v24, -v25
	v_cvt_pk_bf16_f32 v119, -v26, -v27
	v_lshlrev_b32_e32 v52, 16, v164
	v_and_b32_e32 v53, 0xffff0000, v164
	v_mfma_f32_32x32x16_bf16 v[36:51], v[92:95], v[116:119], v[36:51]
	v_lshlrev_b32_e32 v54, 16, v165
	v_and_b32_e32 v55, 0xffff0000, v165
	v_lshlrev_b32_e32 v56, 16, v162
	v_and_b32_e32 v57, 0xffff0000, v162
	v_lshlrev_b32_e32 v58, 16, v163
	v_and_b32_e32 v59, 0xffff0000, v163
	v_lshlrev_b32_e32 v60, 16, v160
	v_and_b32_e32 v61, 0xffff0000, v160
	v_lshlrev_b32_e32 v62, 16, v161
	v_and_b32_e32 v63, 0xffff0000, v161
	v_lshlrev_b32_e32 v64, 16, v156
	v_and_b32_e32 v65, 0xffff0000, v156
	v_lshlrev_b32_e32 v66, 16, v157
	v_and_b32_e32 v67, 0xffff0000, v157
	s_add_i32 s18, s14, s15
	s_ashr_i32 s19, s18, 31
	v_mfma_f32_32x32x16_bf16 v[52:67], v[96:99], v[116:119], v[52:67]
	s_lshl_b64 s[4:5], s[18:19], 2
	v_cvt_pk_bf16_f32 v120, -v4, -v5
	v_cvt_pk_bf16_f32 v121, -v6, -v7
	v_cvt_pk_bf16_f32 v122, -v8, -v9
	v_cvt_pk_bf16_f32 v123, -v10, -v11
	s_add_u32 s8, s12, s4
	s_addc_u32 s9, s13, s5
	s_lshl_b64 s[6:7], s[18:19], 13
	v_mfma_f32_32x32x16_bf16 v[36:51], v[84:87], v[120:123], v[36:51]
	v_lshl_add_u64 v[96:97], v[136:137], 0, s[6:7]
	v_cvt_pk_bf16_f32 v124, -v28, -v29
	v_cvt_pk_bf16_f32 v125, -v30, -v31
	v_lshl_add_u64 v[150:151], v[96:97], 0, v[2:3]
	v_mfma_f32_32x32x16_bf16 v[52:67], v[88:91], v[120:123], v[52:67]
	v_cvt_pk_bf16_f32 v126, -v32, -v33
	global_load_dword v204, v3, s[8:9]
	v_lshl_add_u64 v[152:153], v[96:97], 0, v[142:143]
	global_load_dwordx4 v[96:99], v[150:151], off
	global_load_dwordx4 v[116:119], v[150:151], off offset:32
	s_add_i32 s4, s18, 4
	s_ashr_i32 s5, s4, 31
	s_lshl_b64 s[4:5], s[4:5], 13
	v_cvt_pk_bf16_f32 v127, -v34, -v35
	global_load_dwordx4 v[84:87], v[152:153], off
	global_load_dwordx4 v[128:131], v[152:153], off offset:32
	global_load_dwordx4 v[168:171], v[150:151], off offset:64
	global_load_dwordx4 v[172:175], v[150:151], off offset:96
	global_load_dwordx4 v[176:179], v[152:153], off offset:64
	global_load_dwordx4 v[180:183], v[152:153], off offset:96
	v_lshl_add_u64 v[150:151], v[134:135], 0, s[4:5]
	v_lshl_add_u64 v[88:89], v[146:147], 0, s[4:5]
	v_cvt_pk_bf16_f32 v92, -v12, -v13
	v_cvt_pk_bf16_f32 v93, -v14, -v15
	v_cvt_pk_bf16_f32 v94, -v16, -v17
	v_cvt_pk_bf16_f32 v95, -v18, -v19
	v_lshl_add_u64 v[120:121], v[150:151], 0, v[2:3]
	v_lshl_add_u64 v[196:197], v[150:151], 0, v[142:143]
	global_load_dwordx2 v[158:159], v[88:89], off
	global_load_dwordx2 v[154:155], v[88:89], off offset:16
	global_load_dwordx2 v[152:153], v[88:89], off offset:32
	v_mfma_f32_32x32x16_bf16 v[36:51], v[76:79], v[124:127], v[36:51]
	global_load_dwordx2 v[150:151], v[88:89], off offset:48
	global_load_dwordx2 v[164:165], v[88:89], off offset:64
	global_load_dwordx2 v[162:163], v[88:89], off offset:80
	global_load_dwordx2 v[160:161], v[88:89], off offset:96
	global_load_dwordx2 v[156:157], v[88:89], off offset:112
	global_load_dwordx4 v[76:79], v[120:121], off
	s_nop 0
	global_load_dwordx4 v[88:91], v[120:121], off offset:32
	v_cvt_pk_bf16_f32 v100, v20, v21
	v_cvt_pk_bf16_f32 v101, v22, v23
	v_cvt_pk_bf16_f32 v102, v4, v5
	v_cvt_pk_bf16_f32 v103, v6, v7
	v_cvt_pk_bf16_f32 v104, v24, v25
	v_cvt_pk_bf16_f32 v105, v26, v27
	v_mfma_f32_32x32x16_bf16 v[52:67], v[80:83], v[124:127], v[52:67]
	global_load_dwordx4 v[80:83], v[120:121], off offset:64
	s_nop 0
	global_load_dwordx4 v[120:123], v[120:121], off offset:96
	s_nop 0
	global_load_dwordx4 v[184:187], v[196:197], off
	global_load_dwordx4 v[188:191], v[196:197], off offset:32
	global_load_dwordx4 v[192:195], v[196:197], off offset:64
	s_nop 0
	global_load_dwordx4 v[196:199], v[196:197], off offset:96
	v_lshl_add_u64 v[206:207], v[148:149], 0, s[6:7]
	v_cvt_pk_bf16_f32 v106, v8, v9
	v_cvt_pk_bf16_f32 v107, v10, v11
	v_cvt_pk_bf16_f32 v108, v28, v29
	v_cvt_pk_bf16_f32 v109, v30, v31
	v_cvt_pk_bf16_f32 v110, v12, v13
	v_mfma_f32_32x32x16_bf16 v[36:51], v[68:71], v[92:95], v[36:51]
	v_cvt_pk_bf16_f32 v111, v14, v15
	v_cvt_pk_bf16_f32 v112, v32, v33
	v_cvt_pk_bf16_f32 v113, v34, v35
	v_cvt_pk_bf16_f32 v114, v16, v17
	v_cvt_pk_bf16_f32 v115, v18, v19
	global_store_dwordx2 v[206:207], v[100:101], off
	global_store_dwordx2 v[206:207], v[102:103], off offset:64
	global_store_dwordx2 v[206:207], v[104:105], off offset:16
	global_store_dwordx2 v[206:207], v[106:107], off offset:80
	global_store_dwordx2 v[206:207], v[108:109], off offset:32
	global_store_dwordx2 v[206:207], v[110:111], off offset:96
	global_store_dwordx2 v[206:207], v[112:113], off offset:48
	global_store_dwordx2 v[206:207], v[114:115], off offset:112
	v_mfma_f32_32x32x16_bf16 v[52:67], v[72:75], v[92:95], v[52:67]
	v_cvt_pk_bf16_f32 v36, v36, v37
	v_cvt_pk_bf16_f32 v37, v38, v39
	v_cvt_pk_bf16_f32 v39, v42, v43
	v_cvt_pk_bf16_f32 v42, v48, v49
	v_cvt_pk_bf16_f32 v38, v40, v41
	v_cvt_pk_bf16_f32 v40, v44, v45
	v_cvt_pk_bf16_f32 v43, v50, v51
	s_nop 4
	v_cvt_pk_bf16_f32 v52, v52, v53
	v_cvt_pk_bf16_f32 v53, v54, v55
	v_cvt_pk_bf16_f32 v54, v56, v57
	v_cvt_pk_bf16_f32 v44, v60, v61
	v_cvt_pk_bf16_f32 v45, v62, v63
	v_cvt_pk_bf16_f32 v41, v46, v47
	v_cvt_pk_bf16_f32 v46, v64, v65
	v_lshl_add_u64 v[208:209], v[146:147], 0, s[6:7]
	v_cvt_pk_bf16_f32 v55, v58, v59
	v_cvt_pk_bf16_f32 v47, v66, v67
	global_store_dwordx2 v[208:209], v[36:37], off
	global_store_dwordx2 v[208:209], v[52:53], off offset:64
	global_store_dwordx2 v[208:209], v[38:39], off offset:16
	global_store_dwordx2 v[208:209], v[54:55], off offset:80
	global_store_dwordx2 v[208:209], v[40:41], off offset:32
	global_store_dwordx2 v[208:209], v[44:45], off offset:96
	global_store_dwordx2 v[208:209], v[42:43], off offset:48
	global_store_dwordx2 v[208:209], v[46:47], off offset:112
	s_add_i32 s15, s15, 4
	s_cmpk_lg_i32 s15, 0xfc
	s_waitcnt vmcnt(40)
	v_pk_mul_f32 v[34:35], v[34:35], v[204:205] op_sel_hi:[1,0]
	s_waitcnt vmcnt(39)
	s_waitcnt vmcnt(38)
	v_pk_mul_f32 v[32:33], v[32:33], v[204:205] op_sel_hi:[1,0]
	v_pk_mul_f32 v[30:31], v[30:31], v[204:205] op_sel_hi:[1,0]
	v_pk_mul_f32 v[28:29], v[28:29], v[204:205] op_sel_hi:[1,0]
	s_waitcnt vmcnt(37)
	s_waitcnt vmcnt(35)
	s_waitcnt vmcnt(34)
	v_pk_mul_f32 v[26:27], v[26:27], v[204:205] op_sel_hi:[1,0]
	v_pk_mul_f32 v[24:25], v[24:25], v[204:205] op_sel_hi:[1,0]
	v_pk_mul_f32 v[22:23], v[22:23], v[204:205] op_sel_hi:[1,0]
	s_waitcnt vmcnt(23)
	v_pk_mul_f32 v[20:21], v[20:21], v[204:205] op_sel_hi:[1,0]
	v_pk_mul_f32 v[18:19], v[18:19], v[204:205] op_sel_hi:[1,0]
	v_pk_mul_f32 v[16:17], v[16:17], v[204:205] op_sel_hi:[1,0]
	s_waitcnt vmcnt(20)
	v_cndmask_b32_e32 v60, v120, v122, vcc
	v_cndmask_b32_e32 v61, v121, v123, vcc
	s_waitcnt vmcnt(19)
	v_cndmask_b32_e32 v62, v184, v186, vcc
	v_cndmask_b32_e32 v63, v185, v187, vcc
	v_pk_mul_f32 v[14:15], v[14:15], v[204:205] op_sel_hi:[1,0]
	v_pk_mul_f32 v[12:13], v[12:13], v[204:205] op_sel_hi:[1,0]
	v_pk_mul_f32 v[10:11], v[10:11], v[204:205] op_sel_hi:[1,0]
	v_pk_mul_f32 v[8:9], v[8:9], v[204:205] op_sel_hi:[1,0]
	v_pk_mul_f32 v[6:7], v[6:7], v[204:205] op_sel_hi:[1,0]
	v_pk_mul_f32 v[4:5], v[4:5], v[204:205] op_sel_hi:[1,0]
	ds_bpermute_b32 v145, v166, v60
	ds_bpermute_b32 v167, v166, v61
	ds_bpermute_b32 v203, v166, v62
	ds_bpermute_b32 v204, v166, v63
	s_waitcnt lgkmcnt(0)
	v_mov_b32_e32 v49, v97
	v_mov_b32_e32 v51, v99
	v_mov_b32_e32 v48, v96
	v_mov_b32_e32 v50, v98
	s_nop 1
	v_permlane32_swap_b32_e32 v49, v51
	v_permlane32_swap_b32_e32 v48, v50
	s_nop 1
	s_waitcnt lgkmcnt(0)
	v_mov_b32_e32 v61, v85
	v_mov_b32_e32 v63, v87
	v_mov_b32_e32 v60, v84
	v_mov_b32_e32 v62, v86
	s_nop 1
	v_permlane32_swap_b32_e32 v61, v63
	v_permlane32_swap_b32_e32 v60, v62
	s_nop 1
	v_mfma_f32_32x32x16_bf16 v[20:35], v[48:51], v[36:39], v[20:35]
	s_waitcnt lgkmcnt(0)
	v_mov_b32_e32 v49, v169
	v_mov_b32_e32 v51, v171
	v_mov_b32_e32 v48, v168
	v_mov_b32_e32 v50, v170
	s_nop 1
	v_permlane32_swap_b32_e32 v49, v51
	v_permlane32_swap_b32_e32 v48, v50
	s_nop 1
	v_mfma_f32_32x32x16_bf16 v[4:19], v[60:63], v[36:39], v[4:19]
	s_waitcnt lgkmcnt(0)
	v_mov_b32_e32 v37, v177
	v_mov_b32_e32 v39, v179
	v_mov_b32_e32 v36, v176
	v_mov_b32_e32 v38, v178
	s_nop 1
	v_permlane32_swap_b32_e32 v37, v39
	v_permlane32_swap_b32_e32 v36, v38
	s_nop 1
	v_mfma_f32_32x32x16_bf16 v[20:35], v[48:51], v[52:55], v[20:35]
	s_waitcnt vmcnt(18)
	v_mfma_f32_32x32x16_bf16 v[4:19], v[36:39], v[52:55], v[4:19]
	s_waitcnt vmcnt(17)
	v_mov_b32_e32 v57, v117
	v_mov_b32_e32 v59, v119
	v_mov_b32_e32 v56, v116
	v_mov_b32_e32 v58, v118
	s_nop 1
	v_permlane32_swap_b32_e32 v57, v59
	v_permlane32_swap_b32_e32 v56, v58
	s_nop 1
	s_waitcnt lgkmcnt(0)
	v_mov_b32_e32 v65, v129
	v_mov_b32_e32 v67, v131
	v_mov_b32_e32 v64, v128
	v_mov_b32_e32 v66, v130
	s_nop 1
	v_permlane32_swap_b32_e32 v65, v67
	v_permlane32_swap_b32_e32 v64, v66
	s_nop 1
	v_mfma_f32_32x32x16_bf16 v[20:35], v[56:59], v[40:43], v[20:35]
	v_mov_b32_e32 v69, v173
	v_mov_b32_e32 v71, v175
	v_mov_b32_e32 v68, v172
	v_mov_b32_e32 v70, v174
	s_nop 1
	v_permlane32_swap_b32_e32 v69, v71
	v_permlane32_swap_b32_e32 v68, v70
	s_nop 1
	s_waitcnt lgkmcnt(0)
	v_mov_b32_e32 v61, v181
	v_mov_b32_e32 v63, v183
	v_mov_b32_e32 v60, v180
	v_mov_b32_e32 v62, v182
	s_nop 1
	v_permlane32_swap_b32_e32 v61, v63
	v_permlane32_swap_b32_e32 v60, v62
	s_nop 1
	v_mfma_f32_32x32x16_bf16 v[4:19], v[64:67], v[40:43], v[4:19]
	s_waitcnt vmcnt(16)
	v_mov_b32_e32 v129, v77
	v_mov_b32_e32 v131, v79
	v_mov_b32_e32 v128, v76
	v_mov_b32_e32 v130, v78
	s_nop 1
	v_permlane32_swap_b32_e32 v129, v131
	v_permlane32_swap_b32_e32 v128, v130
	s_nop 1
	v_mfma_f32_32x32x16_bf16 v[20:35], v[68:71], v[44:47], v[20:35]
	s_waitcnt lgkmcnt(0)
	v_mov_b32_e32 v113, v89
	v_mov_b32_e32 v115, v91
	v_mov_b32_e32 v112, v88
	v_mov_b32_e32 v114, v90
	s_nop 1
	v_permlane32_swap_b32_e32 v113, v115
	v_permlane32_swap_b32_e32 v112, v114
	s_nop 1
	s_waitcnt lgkmcnt(0)
	v_mov_b32_e32 v125, v81
	v_mov_b32_e32 v127, v83
	v_mov_b32_e32 v124, v80
	v_mov_b32_e32 v126, v82
	s_nop 1
	v_permlane32_swap_b32_e32 v125, v127
	v_permlane32_swap_b32_e32 v124, v126
	s_nop 1
	v_mfma_f32_32x32x16_bf16 v[4:19], v[60:63], v[44:47], v[4:19]
	v_cndmask_b32_e32 v109, v167, v121, vcc
	v_cndmask_b32_e32 v108, v145, v120, vcc
	v_cndmask_b32_e32 v121, v204, v185, vcc
	v_cndmask_b32_e32 v120, v203, v184, vcc
	s_waitcnt lgkmcnt(0)
	v_mov_b32_e32 v105, v189
	v_mov_b32_e32 v107, v191
	v_mov_b32_e32 v104, v188
	v_mov_b32_e32 v106, v190
	s_nop 1
	v_permlane32_swap_b32_e32 v105, v107
	v_permlane32_swap_b32_e32 v104, v106
	s_nop 1
	s_waitcnt lgkmcnt(0)
	v_mov_b32_e32 v117, v193
	v_mov_b32_e32 v119, v195
	v_mov_b32_e32 v116, v192
	v_mov_b32_e32 v118, v194
	s_nop 1
	v_permlane32_swap_b32_e32 v117, v119
	v_permlane32_swap_b32_e32 v116, v118
	s_nop 1
	s_waitcnt lgkmcnt(0)
	v_mov_b32_e32 v101, v197
	v_mov_b32_e32 v103, v199
	v_mov_b32_e32 v100, v196
	v_mov_b32_e32 v102, v198
	s_nop 1
	v_permlane32_swap_b32_e32 v101, v103
	v_permlane32_swap_b32_e32 v100, v102
	s_nop 1
	v_cndmask_b32_e32 v111, v123, v167, vcc
	v_cndmask_b32_e32 v110, v122, v145, vcc
	v_cndmask_b32_e32 v123, v187, v204, vcc
	v_cndmask_b32_e32 v122, v186, v203, vcc
	v_mov_b64_e32 v[72:73], v[100:101]
	v_mov_b64_e32 v[88:89], v[116:117]
	v_mov_b64_e32 v[80:81], v[104:105]
	v_mov_b64_e32 v[96:97], v[120:121]
	v_mov_b64_e32 v[68:69], v[108:109]
	v_mov_b64_e32 v[84:85], v[124:125]
	v_mov_b64_e32 v[76:77], v[112:113]
	v_mov_b64_e32 v[92:93], v[128:129]
	v_mov_b64_e32 v[74:75], v[102:103]
	v_mov_b64_e32 v[90:91], v[118:119]
	v_mov_b64_e32 v[82:83], v[106:107]
	v_mov_b64_e32 v[98:99], v[122:123]
	v_mov_b64_e32 v[70:71], v[110:111]
	v_mov_b64_e32 v[86:87], v[126:127]
	v_mov_b64_e32 v[78:79], v[114:115]
	v_mov_b64_e32 v[94:95], v[130:131]
	s_cbranch_scc1 .LBB0_800
	v_cvt_pk_bf16_f32 v70, v20, v21
	v_cvt_pk_bf16_f32 v20, -v20, -v21
	v_cvt_pk_bf16_f32 v71, v22, v23
	v_cvt_pk_bf16_f32 v21, -v22, -v23
	v_cvt_pk_bf16_f32 v22, -v24, -v25
	v_lshlrev_b32_e32 v52, 16, v158
	v_and_b32_e32 v53, 0xffff0000, v158
	v_lshlrev_b32_e32 v54, 16, v159
	v_and_b32_e32 v55, 0xffff0000, v159
	v_lshlrev_b32_e32 v56, 16, v154
	v_and_b32_e32 v57, 0xffff0000, v154
	v_lshlrev_b32_e32 v58, 16, v155
	v_and_b32_e32 v59, 0xffff0000, v155
	v_lshlrev_b32_e32 v60, 16, v152
	v_and_b32_e32 v61, 0xffff0000, v152
	v_lshlrev_b32_e32 v62, 16, v153
	v_and_b32_e32 v63, 0xffff0000, v153
	v_lshlrev_b32_e32 v64, 16, v150
	v_and_b32_e32 v65, 0xffff0000, v150
	v_lshlrev_b32_e32 v66, 16, v151
	v_and_b32_e32 v67, 0xffff0000, v151
	v_cvt_pk_bf16_f32 v23, -v26, -v27
	v_lshlrev_b32_e32 v36, 16, v164
	v_and_b32_e32 v37, 0xffff0000, v164
	v_lshlrev_b32_e32 v38, 16, v165
	v_and_b32_e32 v39, 0xffff0000, v165
	v_lshlrev_b32_e32 v40, 16, v162
	v_and_b32_e32 v41, 0xffff0000, v162
	v_lshlrev_b32_e32 v42, 16, v163
	v_and_b32_e32 v43, 0xffff0000, v163
	v_lshlrev_b32_e32 v44, 16, v160
	v_and_b32_e32 v45, 0xffff0000, v160
	v_lshlrev_b32_e32 v46, 16, v161
	v_and_b32_e32 v47, 0xffff0000, v161
	v_lshlrev_b32_e32 v48, 16, v156
	v_and_b32_e32 v49, 0xffff0000, v156
	v_lshlrev_b32_e32 v50, 16, v157
	v_and_b32_e32 v51, 0xffff0000, v157
	v_mfma_f32_32x32x16_bf16 v[52:67], v[128:131], v[20:23], v[52:67]
	v_cvt_pk_bf16_f32 v72, v4, v5
	v_cvt_pk_bf16_f32 v4, -v4, -v5
	v_cvt_pk_bf16_f32 v73, v6, v7
	v_mfma_f32_32x32x16_bf16 v[36:51], v[120:123], v[20:23], v[36:51]
	v_cvt_pk_bf16_f32 v5, -v6, -v7
	v_cvt_pk_bf16_f32 v6, -v8, -v9
	v_cvt_pk_bf16_f32 v7, -v10, -v11
	s_or_b32 s4, s20, s17
	v_mfma_f32_32x32x16_bf16 v[52:67], v[124:127], v[4:7], v[52:67]
	s_or_b32 s4, s4, 0xfc
	s_ashr_i32 s5, s4, 31
	s_lshl_b64 s[14:15], s[4:5], 13
	v_lshl_add_u64 v[68:69], v[148:149], 0, s[14:15]
	global_store_dwordx2 v[68:69], v[70:71], off
	global_store_dwordx2 v[68:69], v[72:73], off offset:64
	v_cvt_pk_bf16_f32 v72, v8, v9
	v_mfma_f32_32x32x16_bf16 v[36:51], v[116:119], v[4:7], v[36:51]
	v_cvt_pk_bf16_f32 v4, -v28, -v29
	v_cvt_pk_bf16_f32 v5, -v30, -v31
	v_cvt_pk_bf16_f32 v6, -v32, -v33
	v_cvt_pk_bf16_f32 v7, -v34, -v35
	v_cvt_pk_bf16_f32 v8, -v12, -v13
	v_mfma_f32_32x32x16_bf16 v[52:67], v[112:115], v[4:7], v[52:67]
	v_cvt_pk_bf16_f32 v73, v10, v11
	v_cvt_pk_bf16_f32 v9, -v14, -v15
	v_cvt_pk_bf16_f32 v10, -v16, -v17
	v_mfma_f32_32x32x16_bf16 v[36:51], v[104:107], v[4:7], v[36:51]
	v_xor_b32_e32 v2, 0x80000000, v18
	v_xor_b32_e32 v11, 0x80000000, v19
	v_cvt_pk_bf16_f32 v11, v2, v11
	v_cvt_pk_bf16_f32 v70, v24, v25
	v_cvt_pk_bf16_f32 v71, v26, v27
	global_store_dwordx2 v[68:69], v[70:71], off offset:16
	global_store_dwordx2 v[68:69], v[72:73], off offset:80
	v_cvt_pk_bf16_f32 v70, v28, v29
	v_mfma_f32_32x32x16_bf16 v[52:67], v[108:111], v[8:11], v[52:67]
	v_cvt_pk_bf16_f32 v71, v30, v31
	v_cvt_pk_bf16_f32 v72, v12, v13
	v_cvt_pk_bf16_f32 v73, v14, v15
	global_store_dwordx2 v[68:69], v[70:71], off offset:32
	global_store_dwordx2 v[68:69], v[72:73], off offset:96
	v_cvt_pk_bf16_f32 v70, v32, v33
	v_cvt_pk_bf16_f32 v71, v34, v35
	v_lshl_add_u64 v[4:5], v[146:147], 0, s[14:15]
	v_mfma_f32_32x32x16_bf16 v[36:51], v[100:103], v[8:11], v[36:51]
	s_nop 2
	v_cvt_pk_bf16_f32 v6, v52, v53
	v_cvt_pk_bf16_f32 v7, v54, v55
	v_cvt_pk_bf16_f32 v72, v16, v17
	v_cvt_pk_bf16_f32 v73, v18, v19
	global_store_dwordx2 v[68:69], v[70:71], off offset:48
	global_store_dwordx2 v[68:69], v[72:73], off offset:112
	s_add_i32 s16, s16, s54
	s_cmp_lt_i32 s16, 64
	s_nop 0
	v_cvt_pk_bf16_f32 v8, v36, v37
	v_cvt_pk_bf16_f32 v9, v38, v39
	global_store_dwordx2 v[4:5], v[6:7], off
	global_store_dwordx2 v[4:5], v[8:9], off offset:64
	v_cvt_pk_bf16_f32 v6, v56, v57
	v_cvt_pk_bf16_f32 v7, v58, v59
	v_cvt_pk_bf16_f32 v8, v40, v41
	v_cvt_pk_bf16_f32 v9, v42, v43
	global_store_dwordx2 v[4:5], v[6:7], off offset:16
	global_store_dwordx2 v[4:5], v[8:9], off offset:80
	v_cvt_pk_bf16_f32 v6, v60, v61
	v_cvt_pk_bf16_f32 v7, v62, v63
	v_cvt_pk_bf16_f32 v8, v44, v45
	v_cvt_pk_bf16_f32 v9, v46, v47
	global_store_dwordx2 v[4:5], v[6:7], off offset:32
	global_store_dwordx2 v[4:5], v[8:9], off offset:96
	v_cvt_pk_bf16_f32 v6, v64, v65
	v_cvt_pk_bf16_f32 v7, v66, v67
	v_cvt_pk_bf16_f32 v8, v48, v49
	v_cvt_pk_bf16_f32 v9, v50, v51
	global_store_dwordx2 v[4:5], v[6:7], off offset:48
	global_store_dwordx2 v[4:5], v[8:9], off offset:112
	s_cbranch_scc1 .LBB0_799
